# placement: whole instruction stream shifted by 4 bytes (one s_nop 0 at kernel entry) on top of v76
# baseline (speedup 1.0000x reference)
_Z3fwd4Args:
	s_nop 0
	s_mov_b32 s96, s2
	s_load_dwordx4 s[44:47], s[0:1], 0xc8
	s_add_u32 s2, s0, 0xd8
	s_addc_u32 s3, s1, 0
	v_readfirstlane_b32 s10, v0
	v_writelane_b32 v252, s2, 0
	s_nop 1
	v_writelane_b32 v252, s3, 1
	s_movk_i32 s2, 0x200
	v_cmp_gt_u32_e32 vcc, s2, v0
	s_and_saveexec_b64 s[4:5], vcc
	v_lshl_add_u32 v1, v0, 2, 0
	v_add_u32_e32 v1, 0x24c00, v1
	v_mov_b32_e32 v2, 0
	ds_write_b32 v1, v2
	s_or_b64 exec, exec, s[4:5]
	s_lshr_b32 s4, s10, 6
	s_cmp_ge_u32 s4, 4
	s_cbranch_scc1 .Lprio_static_done
	s_setprio 1
